# speedup vs baseline: 1.0604x; 1.0523x over previous
.LBB0_20:
	s_or_b64 exec, exec, s[0:1]
	v_lshrrev_b32_e32 v12, 6, v0
	v_bfe_u32 v131, v0, 4, 2
	v_and_b32_e32 v106, 15, v0
	v_lshlrev_b32_e32 v107, 5, v12
	v_or_b32_e32 v73, v107, v106
	v_lshlrev_b32_e32 v60, 5, v131
	v_mov_b32_e32 v61, 0
	v_lshl_add_u64 v[42:43], s[30:31], 0, v[60:61]
	v_lshlrev_b32_e32 v2, 7, v73
	v_mov_b32_e32 v3, v61
	v_lshl_add_u64 v[10:11], v[42:43], 0, v[2:3]
	v_lshl_add_u64 v[50:51], s[18:19], 0, v[60:61]
	global_load_dwordx4 v[2:5], v[10:11], off offset:16
	global_load_dwordx4 v[6:9], v[10:11], off
	v_lshlrev_b32_e32 v10, 9, v73
	v_mov_b32_e32 v11, v61
	v_lshl_add_u64 v[34:35], v[50:51], 0, v[10:11]
	v_lshlrev_b32_e32 v62, 7, v12
	v_mov_b32_e32 v63, v61
	v_lshl_add_u64 v[18:19], v[34:35], 0, v[62:63]
	global_load_dwordx4 v[10:13], v[18:19], off offset:16
	global_load_dwordx4 v[14:17], v[18:19], off
	v_add_u32_e32 v18, 32, v107
	v_and_b32_e32 v108, 0x60, v18
	v_lshlrev_b32_e32 v64, 2, v108
	v_mov_b32_e32 v65, v61
	v_lshl_add_u64 v[26:27], v[34:35], 0, v[64:65]
	v_xor_b32_e32 v109, 64, v107
	global_load_dwordx4 v[18:21], v[26:27], off offset:16
	global_load_dwordx4 v[22:25], v[26:27], off
	v_lshlrev_b32_e32 v66, 2, v109
	v_mov_b32_e32 v67, v61
	v_lshl_add_u64 v[36:37], v[34:35], 0, v[66:67]
	global_load_dwordx4 v[26:29], v[36:37], off
	global_load_dwordx4 v[30:33], v[36:37], off offset:16
	v_add_u32_e32 v36, 0x60, v107
	v_and_b32_e32 v111, 0x60, v36
	v_mov_b32_e32 v69, v61
	v_lshlrev_b32_e32 v68, 2, v111
	v_lshl_add_u64 v[44:45], v[34:35], 0, v[68:69]
	global_load_dwordx4 v[34:37], v[44:45], off
	global_load_dwordx4 v[38:41], v[44:45], off offset:16
	v_or_b32_e32 v54, 16, v73
	v_mov_b32_e32 v45, v61
	v_lshlrev_b32_e32 v44, 7, v54
	v_lshl_add_u64 v[52:53], v[42:43], 0, v[44:45]
	global_load_dwordx4 v[42:45], v[52:53], off
	global_load_dwordx4 v[46:49], v[52:53], off offset:16
	v_mov_b32_e32 v53, v61
	v_lshlrev_b32_e32 v52, 9, v54
	v_lshl_add_u64 v[58:59], v[50:51], 0, v[52:53]
	v_lshl_add_u64 v[70:71], v[58:59], 0, v[62:63]
	global_load_dwordx4 v[50:53], v[70:71], off
	global_load_dwordx4 v[54:57], v[70:71], off offset:16
	v_lshl_add_u64 v[70:71], v[58:59], 0, v[64:65]
	v_lshl_add_u64 v[98:99], v[58:59], 0, v[66:67]
	v_lshl_add_u64 v[58:59], v[58:59], 0, v[68:69]
	global_load_dwordx4 v[74:77], v[70:71], off offset:16
	global_load_dwordx4 v[78:81], v[70:71], off
	global_load_dwordx4 v[82:85], v[98:99], off offset:16
	global_load_dwordx4 v[86:89], v[98:99], off
	global_load_dwordx4 v[90:93], v[58:59], off offset:16
	global_load_dwordx4 v[94:97], v[58:59], off
	s_mov_b32 s0, 0x3fb8aa3b
	v_lshlrev_b32_e32 v72, 9, v0
	v_and_b32_e32 v1, 16, v1
	v_or3_b32 v107, v106, v1, v107
	v_lshlrev_b32_e32 v107, 1, v107
	s_mov_b32 s3, 32
	v_cmp_eq_u32_e64 s[4:5], 3, v131
	s_waitcnt vmcnt(19)
	v_pk_mul_f32 v[58:59], v[2:3], s[0:1] op_sel_hi:[1,0]
	s_waitcnt vmcnt(18)
	v_pk_mul_f32 v[6:7], v[6:7], s[0:1] op_sel_hi:[1,0]
	v_pk_mul_f32 v[8:9], v[8:9], s[0:1] op_sel_hi:[1,0]
	v_cvt_pk_f16_f32 v2, v6, v7
	v_cvt_pk_f16_f32 v3, v8, v9
	v_pk_mul_f32 v[70:71], v[4:5], s[0:1] op_sel_hi:[1,0]
	v_cvt_pk_f16_f32 v4, v58, v59
	s_waitcnt vmcnt(17)
	v_cvt_f16_f32_e32 v13, v13
	s_waitcnt vmcnt(16)
	v_cvt_f16_f32_e32 v6, v14
	v_cvt_pk_f16_f32 v8, v17, v10
	v_cvt_pk_f16_f32 v5, v70, v71
	v_lshl_add_u64 v[70:71], s[22:23], 0, v[60:61]
	v_and_b32_e32 v60, 0x19e00, v72
	v_cvt_pk_f16_f32 v9, v15, v16
	s_waitcnt vmcnt(15)
	v_cvt_f16_f32_e32 v17, v21
	v_cvt_pk_f16_f32 v10, v11, v12
	s_waitcnt vmcnt(14)
	v_cvt_f16_f32_e32 v14, v22
	v_cvt_pk_f16_f32 v15, v23, v24
	v_cvt_pk_f16_f32 v12, v25, v18
	v_cvt_pk_f16_f32 v16, v19, v20
	v_lshl_add_u64 v[58:59], v[70:71], 0, v[60:61]
	s_waitcnt vmcnt(13)
	v_cvt_f16_f32_e32 v18, v26
	v_alignbit_b32 v7, v8, v9, 16
	v_alignbit_b32 v11, v12, v15, 16
	v_alignbit_b32 v12, v16, v12, 16
	v_pack_b32_f16 v6, v6, v9
	v_alignbit_b32 v9, v13, v10, 16
	v_alignbit_b32 v13, v17, v16, 16
	v_lshl_add_u64 v[16:17], v[58:59], 0, v[62:63]
	global_load_dwordx4 v[98:101], v[16:17], off offset:16
	global_load_dwordx4 v[102:105], v[16:17], off
	s_waitcnt vmcnt(14)
	v_cvt_f16_f32_e32 v17, v33
	s_waitcnt vmcnt(13)
	v_cvt_f16_f32_e32 v20, v34
	v_alignbit_b32 v8, v10, v8, 16
	v_pack_b32_f16 v10, v14, v15
	v_cvt_pk_f16_f32 v15, v27, v28
	v_pack_b32_f16 v14, v18, v15
	v_cvt_pk_f16_f32 v18, v29, v30
	v_cvt_pk_f16_f32 v19, v31, v32
	v_alignbit_b32 v16, v19, v18, 16
	v_alignbit_b32 v17, v17, v19, 16
	v_cvt_pk_f16_f32 v19, v35, v36
	v_alignbit_b32 v15, v18, v15, 16
	v_pack_b32_f16 v18, v20, v19
	v_lshl_add_u64 v[20:21], v[58:59], 0, v[64:65]
	global_load_dwordx4 v[112:115], v[20:21], off offset:16
	global_load_dwordx4 v[116:119], v[20:21], off
	s_waitcnt vmcnt(14)
	v_cvt_f16_f32_e32 v21, v41
	v_lshl_add_u64 v[26:27], v[58:59], 0, v[66:67]
	global_load_dwordx4 v[124:127], v[26:27], off offset:16
	global_load_dwordx4 v[132:135], v[26:27], off
	v_cvt_pk_f16_f32 v20, v37, v38
	v_cvt_pk_f16_f32 v22, v39, v40
	s_waitcnt vmcnt(13)
	v_cvt_f16_f32_e32 v28, v50
	v_alignbit_b32 v19, v20, v19, 16
	v_alignbit_b32 v20, v22, v20, 16
	v_alignbit_b32 v21, v21, v22, 16
	v_pk_mul_f32 v[22:23], v[42:43], s[0:1] op_sel_hi:[1,0]
	v_pk_mul_f32 v[24:25], v[44:45], s[0:1] op_sel_hi:[1,0]
	v_cvt_pk_f16_f32 v22, v22, v23
	v_cvt_pk_f16_f32 v23, v24, v25
	v_pk_mul_f32 v[24:25], v[46:47], s[0:1] op_sel_hi:[1,0]
	v_pk_mul_f32 v[26:27], v[48:49], s[0:1] op_sel_hi:[1,0]
	v_cvt_pk_f16_f32 v24, v24, v25
	v_cvt_pk_f16_f32 v25, v26, v27
	v_cvt_pk_f16_f32 v27, v51, v52
	s_waitcnt vmcnt(12)
	v_cvt_f16_f32_e32 v31, v57
	v_pack_b32_f16 v26, v28, v27
	v_lshl_add_u64 v[28:29], v[58:59], 0, v[68:69]
	global_load_dwordx4 v[140:143], v[28:29], off offset:16
	global_load_dwordx4 v[144:147], v[28:29], off
	s_mov_b64 s[0:1], 0x2000
	v_cvt_pk_f16_f32 v30, v53, v54
	v_cvt_pk_f16_f32 v29, v55, v56
	v_lshl_add_u64 v[46:47], v[58:59], 0, s[0:1]
	v_alignbit_b32 v27, v30, v27, 16
	v_alignbit_b32 v28, v29, v30, 16
	v_alignbit_b32 v29, v31, v29, 16
	v_lshl_add_u64 v[30:31], v[46:47], 0, v[62:63]
	global_load_dwordx4 v[148:151], v[30:31], off offset:16
	global_load_dwordx4 v[152:155], v[30:31], off
	s_waitcnt vmcnt(14)
	v_cvt_f16_f32_e32 v32, v78
	v_cvt_f16_f32_e32 v33, v77
	s_waitcnt vmcnt(12)
	v_cvt_f16_f32_e32 v35, v86
	v_cvt_pk_f16_f32 v31, v79, v80
	v_pack_b32_f16 v30, v32, v31
	v_cvt_pk_f16_f32 v32, v81, v74
	v_cvt_pk_f16_f32 v34, v75, v76
	v_cvt_pk_f16_f32 v36, v87, v88
	v_cvt_pk_f16_f32 v38, v89, v82
	v_alignbit_b32 v31, v32, v31, 16
	v_alignbit_b32 v32, v34, v32, 16
	v_alignbit_b32 v33, v33, v34, 16
	v_pack_b32_f16 v34, v35, v36
	v_alignbit_b32 v35, v38, v36, 16
	v_lshl_add_u64 v[36:37], v[46:47], 0, v[64:65]
	global_load_dwordx4 v[74:77], v[36:37], off offset:16
	global_load_dwordx4 v[78:81], v[36:37], off
	v_cvt_f16_f32_e32 v37, v85
	s_waitcnt vmcnt(12)
	v_cvt_f16_f32_e32 v40, v94
	v_cvt_f16_f32_e32 v44, v93
	v_cvt_pk_f16_f32 v39, v83, v84
	v_alignbit_b32 v36, v39, v38, 16
	v_alignbit_b32 v37, v37, v39, 16
	v_cvt_pk_f16_f32 v39, v95, v96
	v_pack_b32_f16 v38, v40, v39
	v_cvt_pk_f16_f32 v42, v97, v90
	v_cvt_pk_f16_f32 v43, v91, v92
	v_lshl_add_u64 v[40:41], v[46:47], 0, v[66:67]
	v_alignbit_b32 v39, v42, v39, 16
	global_load_dwordx4 v[82:85], v[40:41], off offset:16
	global_load_dwordx4 v[86:89], v[40:41], off
	v_alignbit_b32 v40, v43, v42, 16
	v_alignbit_b32 v41, v44, v43, 16
	v_lshl_add_u64 v[46:47], v[46:47], 0, v[68:69]
	s_mov_b64 s[0:1], 0x4000
	s_waitcnt vmcnt(12)
	v_pk_add_f32 v[42:43], v[102:103], v[102:103]
	v_pk_add_f32 v[44:45], v[104:105], v[104:105]
	v_cvt_pk_f16_f32 v42, v42, v43
	v_cvt_pk_f16_f32 v43, v44, v45
	v_pk_add_f32 v[44:45], v[98:99], v[98:99]
	global_load_dwordx4 v[90:93], v[46:47], off offset:16
	global_load_dwordx4 v[94:97], v[46:47], off
	v_pk_add_f32 v[46:47], v[100:101], v[100:101]
	v_lshl_add_u64 v[120:121], v[58:59], 0, s[0:1]
	v_cvt_pk_f16_f32 v44, v44, v45
	v_cvt_pk_f16_f32 v45, v46, v47
	v_lshl_add_u64 v[50:51], v[120:121], 0, v[62:63]
	global_load_dwordx4 v[98:101], v[50:51], off offset:16
	global_load_dwordx4 v[102:105], v[50:51], off
	v_lshl_add_u64 v[58:59], v[120:121], 0, v[66:67]
	v_or_b32_e32 v60, 0x6000, v72
	s_waitcnt vmcnt(15)
	v_pk_add_f32 v[50:51], v[114:115], v[114:115]
	s_waitcnt vmcnt(14)
	v_pk_add_f32 v[46:47], v[116:117], v[116:117]
	v_pk_add_f32 v[48:49], v[118:119], v[118:119]
	v_cvt_pk_f16_f32 v46, v46, v47
	v_cvt_pk_f16_f32 v47, v48, v49
	v_pk_add_f32 v[48:49], v[112:113], v[112:113]
	s_waitcnt vmcnt(12)
	v_pk_add_f32 v[52:53], v[134:135], v[134:135]
	v_cvt_pk_f16_f32 v48, v48, v49
	v_cvt_pk_f16_f32 v49, v50, v51
	v_pk_add_f32 v[50:51], v[132:133], v[132:133]
	v_pk_add_f32 v[54:55], v[126:127], v[126:127]
	v_cvt_pk_f16_f32 v50, v50, v51
	v_cvt_pk_f16_f32 v51, v52, v53
	v_pk_add_f32 v[52:53], v[124:125], v[124:125]
	v_lshl_add_u64 v[70:71], v[70:71], 0, v[60:61]
	v_cvt_pk_f16_f32 v52, v52, v53
	v_cvt_pk_f16_f32 v53, v54, v55
	v_lshl_add_u64 v[54:55], v[120:121], 0, v[64:65]
	global_load_dwordx4 v[112:115], v[54:55], off offset:16
	global_load_dwordx4 v[116:119], v[54:55], off
	global_load_dwordx4 v[124:127], v[58:59], off offset:16
	global_load_dwordx4 v[132:135], v[58:59], off
	v_lshl_add_u64 v[120:121], v[120:121], 0, v[68:69]
	v_lshl_add_u64 v[60:61], v[70:71], 0, v[62:63]
	s_waitcnt vmcnt(15)
	v_pk_add_f32 v[58:59], v[142:143], v[142:143]
	s_waitcnt vmcnt(14)
	v_pk_add_f32 v[54:55], v[144:145], v[144:145]
	v_pk_add_f32 v[56:57], v[146:147], v[146:147]
	v_cvt_pk_f16_f32 v54, v54, v55
	v_cvt_pk_f16_f32 v55, v56, v57
	v_pk_add_f32 v[56:57], v[140:141], v[140:141]
	global_load_dwordx4 v[140:143], v[120:121], off offset:16
	global_load_dwordx4 v[144:147], v[120:121], off
	v_cvt_pk_f16_f32 v56, v56, v57
	v_cvt_pk_f16_f32 v57, v58, v59
	v_lshl_add_u64 v[64:65], v[70:71], 0, v[64:65]
	s_waitcnt vmcnt(14)
	v_pk_add_f32 v[58:59], v[152:153], v[152:153]
	v_pk_add_f32 v[120:121], v[154:155], v[154:155]
	global_load_dwordx4 v[152:155], v[60:61], off offset:16
	global_load_dwordx4 v[156:159], v[60:61], off
	v_cvt_pk_f16_f32 v58, v58, v59
	v_cvt_pk_f16_f32 v59, v120, v121
	v_pk_add_f32 v[120:121], v[148:149], v[148:149]
	v_pk_add_f32 v[62:63], v[150:151], v[150:151]
	global_load_dwordx4 v[148:151], v[64:65], off offset:16
	global_load_dwordx4 v[160:163], v[64:65], off
	v_lshl_add_u64 v[66:67], v[70:71], 0, v[66:67]
	global_load_dwordx4 v[164:167], v[66:67], off offset:16
	global_load_dwordx4 v[168:171], v[66:67], off
	v_lshl_add_u64 v[68:69], v[70:71], 0, v[68:69]
	global_load_dwordx4 v[172:175], v[68:69], off offset:16
	global_load_dwordx4 v[176:179], v[68:69], off
	v_cvt_pk_f16_f32 v60, v120, v121
	v_cvt_pk_f16_f32 v61, v62, v63
	v_lshlrev_b32_e32 v120, 2, v73
	v_and_b32_e32 v73, 0xcf, v0
	s_waitcnt vmcnt(20)
	v_pk_add_f32 v[62:63], v[78:79], v[78:79]
	v_pk_add_f32 v[64:65], v[80:81], v[80:81]
	v_cvt_pk_f16_f32 v62, v62, v63
	v_cvt_pk_f16_f32 v63, v64, v65
	v_pk_add_f32 v[64:65], v[74:75], v[74:75]
	v_pk_add_f32 v[74:75], v[76:77], v[76:77]
	v_lshlrev_b32_e32 v76, 2, v73
	v_mov_b32_e32 v77, 0xc0
	global_load_dword v110, v120, s[20:21]
	global_load_dword v121, v120, s[20:21] offset:64
	global_load_dword v122, v76, s[8:9]
	v_lshl_or_b32 v77, v0, 2, v77
	global_load_dword v128, v76, s[8:9] offset:64
	global_load_dword v129, v76, s[8:9] offset:128
	global_load_dword v130, v77, s[8:9]
	v_cvt_pk_f16_f32 v64, v64, v65
	v_cvt_pk_f16_f32 v65, v74, v75
	s_waitcnt vmcnt(24)
	v_pk_add_f32 v[66:67], v[86:87], v[86:87]
	v_pk_add_f32 v[74:75], v[88:89], v[88:89]
	v_pk_add_f32 v[68:69], v[82:83], v[82:83]
	v_pk_add_f32 v[70:71], v[84:85], v[84:85]
	v_cvt_pk_f16_f32 v66, v66, v67
	v_cvt_pk_f16_f32 v67, v74, v75
	v_cvt_pk_f16_f32 v68, v68, v69
	v_cvt_pk_f16_f32 v69, v70, v71
	s_movk_i32 s0, 0xc0
	s_waitcnt vmcnt(22)
	v_pk_add_f32 v[70:71], v[94:95], v[94:95]
	v_pk_add_f32 v[74:75], v[96:97], v[96:97]
	v_cvt_pk_f16_f32 v70, v70, v71
	v_cvt_pk_f16_f32 v71, v74, v75
	v_pk_add_f32 v[74:75], v[90:91], v[90:91]
	s_waitcnt vmcnt(21)
	v_pk_add_f32 v[78:79], v[100:101], v[100:101]
	v_cvt_pk_f16_f32 v72, v74, v75
	v_pk_add_f32 v[74:75], v[92:93], v[92:93]
	s_waitcnt vmcnt(20)
	v_pk_add_f32 v[76:77], v[104:105], v[104:105]
	v_cvt_pk_f16_f32 v73, v74, v75
	v_pk_add_f32 v[74:75], v[102:103], v[102:103]
	v_mov_b32_e32 v186, 0
	v_mov_b32_e32 v187, 0
	v_mov_b32_e32 v188, 0
	v_mov_b32_e32 v189, 0
	v_mov_b32_e32 v190, 0x13480
	ds_write_b128 v190, v[186:189]
	s_waitcnt lgkmcnt(0)
	v_cvt_pk_f16_f32 v74, v74, v75
	v_cvt_pk_f16_f32 v75, v76, v77
	v_pk_add_f32 v[76:77], v[98:99], v[98:99]
	s_barrier
	v_cvt_pk_f16_f32 v76, v76, v77
	v_cvt_pk_f16_f32 v77, v78, v79
	s_waitcnt vmcnt(19)
	v_pk_add_f32 v[82:83], v[114:115], v[114:115]
	s_waitcnt vmcnt(18)
	v_pk_add_f32 v[78:79], v[116:117], v[116:117]
	v_pk_add_f32 v[80:81], v[118:119], v[118:119]
	v_cvt_pk_f16_f32 v78, v78, v79
	v_cvt_pk_f16_f32 v79, v80, v81
	v_pk_add_f32 v[80:81], v[112:113], v[112:113]
	s_waitcnt vmcnt(16)
	v_pk_add_f32 v[84:85], v[134:135], v[134:135]
	v_cvt_pk_f16_f32 v80, v80, v81
	v_cvt_pk_f16_f32 v81, v82, v83
	v_pk_add_f32 v[82:83], v[132:133], v[132:133]
	v_pk_add_f32 v[86:87], v[126:127], v[126:127]
	v_cvt_pk_f16_f32 v82, v82, v83
	v_cvt_pk_f16_f32 v83, v84, v85
	v_pk_add_f32 v[84:85], v[124:125], v[124:125]
	s_waitcnt vmcnt(14)
	v_pk_add_f32 v[88:89], v[146:147], v[146:147]
	v_cvt_pk_f16_f32 v84, v84, v85
	v_cvt_pk_f16_f32 v85, v86, v87
	v_pk_add_f32 v[86:87], v[144:145], v[144:145]
	v_pk_add_f32 v[90:91], v[142:143], v[142:143]
	v_cvt_pk_f16_f32 v86, v86, v87
	v_cvt_pk_f16_f32 v87, v88, v89
	v_pk_add_f32 v[88:89], v[140:141], v[140:141]
	s_waitcnt vmcnt(12)
	v_pk_add_f32 v[92:93], v[158:159], v[158:159]
	v_cvt_pk_f16_f32 v88, v88, v89
	v_cvt_pk_f16_f32 v89, v90, v91
	v_pk_add_f32 v[90:91], v[156:157], v[156:157]
	v_pk_add_f32 v[94:95], v[154:155], v[154:155]
	v_cvt_pk_f16_f32 v90, v90, v91
	v_cvt_pk_f16_f32 v91, v92, v93
	v_pk_add_f32 v[92:93], v[152:153], v[152:153]
	s_waitcnt vmcnt(10)
	v_pk_add_f32 v[96:97], v[162:163], v[162:163]
	v_cvt_pk_f16_f32 v92, v92, v93
	v_cvt_pk_f16_f32 v93, v94, v95
	v_pk_add_f32 v[94:95], v[160:161], v[160:161]
	v_pk_add_f32 v[98:99], v[150:151], v[150:151]
	v_cvt_pk_f16_f32 v94, v94, v95
	v_cvt_pk_f16_f32 v95, v96, v97
	v_pk_add_f32 v[96:97], v[148:149], v[148:149]
	s_waitcnt vmcnt(8)
	v_pk_add_f32 v[100:101], v[170:171], v[170:171]
	v_cvt_pk_f16_f32 v96, v96, v97
	v_cvt_pk_f16_f32 v97, v98, v99
	v_pk_add_f32 v[98:99], v[168:169], v[168:169]
	v_pk_add_f32 v[102:103], v[166:167], v[166:167]
	v_cvt_pk_f16_f32 v98, v98, v99
	v_cvt_pk_f16_f32 v99, v100, v101
	v_pk_add_f32 v[100:101], v[164:165], v[164:165]
	s_waitcnt vmcnt(6)
	v_pk_add_f32 v[104:105], v[178:179], v[178:179]
	v_cvt_pk_f16_f32 v100, v100, v101
	v_cvt_pk_f16_f32 v101, v102, v103
	v_pk_add_f32 v[102:103], v[176:177], v[176:177]
	v_lshlrev_b32_e32 v115, 4, v131
	v_cvt_pk_f16_f32 v102, v102, v103
	v_cvt_pk_f16_f32 v103, v104, v105
	v_pk_add_f32 v[104:105], v[172:173], v[172:173]
	v_pk_add_f32 v[112:113], v[174:175], v[174:175]
	v_and_or_b32 v116, v0, s0, v115
	v_cvt_pk_f16_f32 v104, v104, v105
	v_cvt_pk_f16_f32 v105, v112, v113
	v_or_b32_e32 v1, v116, v106
	v_add_u32_e32 v112, 0x129c0, v120
	ds_read2_b32 v[112:113], v112 offset1:16
	v_lshrrev_b32_e32 v117, 3, v1
	v_mov_b32_e32 v1, 0x133c0
	v_lshl_or_b32 v108, v108, 1, v115
	v_lshl_or_b32 v109, v109, 1, v115
	v_lshl_or_b32 v111, v111, 1, v115
	v_add_u32_e32 v148, 0x131c0, v107
	v_add_u32_e32 v149, 0x132c0, v107
	v_mov_b32_e32 v107, 0x13440
	v_lshl_add_u32 v1, v117, 2, v1
	v_add_u32_e32 v139, 0x131c0, v116
	v_add_u32_e32 v140, 0x131c0, v108
	v_add_u32_e32 v141, 0x131c0, v109
	v_add_u32_e32 v142, 0x131c0, v111
	v_add_u32_e32 v143, 0x132c0, v116
	v_add_u32_e32 v144, 0x132c0, v108
	v_add_u32_e32 v145, 0x132c0, v109
	v_add_u32_e32 v146, 0x132c0, v111
	v_or_b32_e32 v147, 0x13440, v115
	v_lshl_or_b32 v150, v117, 1, v107
	v_lshlrev_b32_e32 v151, 2, v123
	ds_read_b32 v152, v1
	ds_read_b32 v153, v151
	s_waitcnt vmcnt(5)
	v_mul_f32_e32 v106, 0x3fb8aa3b, v110
	s_waitcnt vmcnt(4)
	v_mul_f32_e32 v110, 0x3fb8aa3b, v121
	s_waitcnt vmcnt(3)
	v_mul_f32_e32 v114, 0x4038aa3b, v122
	s_waitcnt vmcnt(2)
	v_mul_f32_e32 v118, 0x4038aa3b, v128
	s_waitcnt vmcnt(1)
	v_mul_f32_e32 v122, 0x4038aa3b, v129
	s_waitcnt vmcnt(0)
	v_mul_f32_e32 v126, 0x4038aa3b, v130
	s_waitcnt lgkmcnt(2)
	v_mul_f32_e32 v130, 0x3fb8aa3b, v112
	v_mul_f32_e32 v134, 0x3fb8aa3b, v113
	v_cmp_lt_u32_e64 s[0:1], 1, v131
	v_and_b32_e32 v132, 16, v0
	v_mov_b32_e32 v107, 0
	v_cndmask_b32_e64 v154, v130, v134, s[0:1]
	v_mov_b32_e32 v108, 0
	v_mov_b32_e32 v109, 0
	v_mov_b32_e32 v111, 0
	v_mov_b32_e32 v112, 0
	v_mov_b32_e32 v113, 0
	v_mov_b32_e32 v115, 0
	v_mov_b32_e32 v116, 0
	v_mov_b32_e32 v117, 0
	v_mov_b32_e32 v119, 0
	v_mov_b32_e32 v120, 0
	v_mov_b32_e32 v121, 0
	v_mov_b32_e32 v123, 0
	v_mov_b32_e32 v124, 0
	v_mov_b32_e32 v125, 0
	v_mov_b32_e32 v127, 0
	v_mov_b32_e32 v128, 0
	v_mov_b32_e32 v129, 0
	v_cmp_eq_u32_e64 s[6:7], 0, v132
	v_mov_b32_e32 v135, 0
	v_mov_b32_e32 v136, 0
	v_mov_b32_e32 v137, 0
	v_mov_b32_e32 v131, 0
	v_mov_b32_e32 v132, 0
	v_mov_b32_e32 v133, 0
	v_and_b32_e32 v186, 3, v0
	v_and_b32_e32 v187, 2, v0
	v_and_b32_e32 v188, 1, v0
	v_cmp_ne_u32_e64 s[44:45], 0, v186
	v_cmp_ne_u32_e64 s[46:47], 0, v187
	v_cmp_ne_u32_e64 s[48:49], 0, v188
	v_mov_b32_e32 v189, 0x44444444
	v_mov_b32_e32 v191, 0xeeeeeeee
	v_cndmask_b32_e64 v147, v147, v190, s[44:45]
	v_cndmask_b32_e64 v191, v189, v191, s[48:49]
	v_cndmask_b32_e64 v139, v139, v140, s[48:49]
	v_cndmask_b32_e64 v141, v141, v142, s[48:49]
	v_cndmask_b32_e64 v139, v139, v190, s[46:47]
	v_cndmask_b32_e64 v141, v141, v190, s[46:47]
	v_cndmask_b32_e64 v143, v143, v144, s[48:49]
	v_cndmask_b32_e64 v145, v145, v146, s[48:49]
	v_cndmask_b32_e64 v143, v143, v190, s[46:47]
	v_cndmask_b32_e64 v145, v145, v190, s[46:47]
	v_mov_b32_e32 v192, 0
	v_mov_b32_e32 v193, 0
	v_mov_b32_e32 v194, 0
	v_mov_b32_e32 v195, 0
	v_mov_b32_e32 v196, 0
	v_mov_b32_e32 v197, 0
	v_mov_b32_e32 v198, 0
	v_mov_b32_e32 v199, 0
	v_mov_b32_e32 v200, 0
	v_mov_b32_e32 v201, 0
	v_mov_b32_e32 v202, 0
	v_mov_b32_e32 v203, 0
	v_mov_b32_e32 v204, 0
	v_mov_b32_e32 v205, 0
	v_mov_b32_e32 v206, 0
	v_mov_b32_e32 v207, 0
	v_mov_b32_e32 v208, 0
	v_mov_b32_e32 v209, 0
	v_mov_b32_e32 v210, 0
	v_mov_b32_e32 v211, 0
	v_mov_b32_e32 v212, 0
	v_mov_b32_e32 v213, 0
	v_mov_b32_e32 v214, 0
	v_mov_b32_e32 v215, 0
	v_and_b32_e32 v224, 15, v0
	v_bfe_u32 v225, v0, 5, 1
	v_lshl_add_u32 v226, v225, 4, v224
	v_lshlrev_b32_e32 v226, 2, v226
	v_add_u32_e32 v227, 128, v226
	v_and_b32_e32 v225, 16, v0
	v_cmp_ne_u32_e64 s[50:51], 0, v225
	ds_bpermute_b32 v244, v226, v6
	ds_bpermute_b32 v245, v226, v8
	s_waitcnt lgkmcnt(0)
	v_cndmask_b32_e64 v228, v244, v245, s[50:51]
	ds_bpermute_b32 v244, v226, v10
	ds_bpermute_b32 v245, v226, v12
	s_waitcnt lgkmcnt(0)
	v_cndmask_b32_e64 v229, v244, v245, s[50:51]
	ds_bpermute_b32 v244, v226, v7
	ds_bpermute_b32 v245, v226, v9
	s_waitcnt lgkmcnt(0)
	v_cndmask_b32_e64 v230, v244, v245, s[50:51]
	ds_bpermute_b32 v244, v226, v11
	ds_bpermute_b32 v245, v226, v13
	s_waitcnt lgkmcnt(0)
	v_cndmask_b32_e64 v231, v244, v245, s[50:51]
	ds_bpermute_b32 v244, v227, v6
	ds_bpermute_b32 v245, v227, v8
	s_waitcnt lgkmcnt(0)
	v_cndmask_b32_e64 v232, v244, v245, s[50:51]
	ds_bpermute_b32 v244, v227, v10
	ds_bpermute_b32 v245, v227, v12
	s_waitcnt lgkmcnt(0)
	v_cndmask_b32_e64 v233, v244, v245, s[50:51]
	ds_bpermute_b32 v244, v227, v7
	ds_bpermute_b32 v245, v227, v9
	s_waitcnt lgkmcnt(0)
	v_cndmask_b32_e64 v234, v244, v245, s[50:51]
	ds_bpermute_b32 v244, v227, v11
	ds_bpermute_b32 v245, v227, v13
	s_waitcnt lgkmcnt(0)
	v_cndmask_b32_e64 v235, v244, v245, s[50:51]
	v_mov_b32_e32 v6, v228
	v_mov_b32_e32 v7, v229
	v_mov_b32_e32 v8, v230
	v_mov_b32_e32 v9, v231
	v_mov_b32_e32 v10, v232
	v_mov_b32_e32 v11, v233
	v_mov_b32_e32 v12, v234
	v_mov_b32_e32 v13, v235
	ds_bpermute_b32 v244, v226, v14
	ds_bpermute_b32 v245, v226, v16
	s_waitcnt lgkmcnt(0)
	v_cndmask_b32_e64 v228, v244, v245, s[50:51]
	ds_bpermute_b32 v244, v226, v18
	ds_bpermute_b32 v245, v226, v20
	s_waitcnt lgkmcnt(0)
	v_cndmask_b32_e64 v229, v244, v245, s[50:51]
	ds_bpermute_b32 v244, v226, v15
	ds_bpermute_b32 v245, v226, v17
	s_waitcnt lgkmcnt(0)
	v_cndmask_b32_e64 v230, v244, v245, s[50:51]
	ds_bpermute_b32 v244, v226, v19
	ds_bpermute_b32 v245, v226, v21
	s_waitcnt lgkmcnt(0)
	v_cndmask_b32_e64 v231, v244, v245, s[50:51]
	ds_bpermute_b32 v244, v227, v14
	ds_bpermute_b32 v245, v227, v16
	s_waitcnt lgkmcnt(0)
	v_cndmask_b32_e64 v232, v244, v245, s[50:51]
	ds_bpermute_b32 v244, v227, v18
	ds_bpermute_b32 v245, v227, v20
	s_waitcnt lgkmcnt(0)
	v_cndmask_b32_e64 v233, v244, v245, s[50:51]
	ds_bpermute_b32 v244, v227, v15
	ds_bpermute_b32 v245, v227, v17
	s_waitcnt lgkmcnt(0)
	v_cndmask_b32_e64 v234, v244, v245, s[50:51]
	ds_bpermute_b32 v244, v227, v19
	ds_bpermute_b32 v245, v227, v21
	s_waitcnt lgkmcnt(0)
	v_cndmask_b32_e64 v235, v244, v245, s[50:51]
	v_mov_b32_e32 v14, v228
	v_mov_b32_e32 v15, v229
	v_mov_b32_e32 v16, v230
	v_mov_b32_e32 v17, v231
	v_mov_b32_e32 v18, v232
	v_mov_b32_e32 v19, v233
	v_mov_b32_e32 v20, v234
	v_mov_b32_e32 v21, v235
	ds_bpermute_b32 v244, v226, v26
	ds_bpermute_b32 v245, v226, v28
	s_waitcnt lgkmcnt(0)
	v_cndmask_b32_e64 v228, v244, v245, s[50:51]
	ds_bpermute_b32 v244, v226, v30
	ds_bpermute_b32 v245, v226, v32
	s_waitcnt lgkmcnt(0)
	v_cndmask_b32_e64 v229, v244, v245, s[50:51]
	ds_bpermute_b32 v244, v226, v27
	ds_bpermute_b32 v245, v226, v29
	s_waitcnt lgkmcnt(0)
	v_cndmask_b32_e64 v230, v244, v245, s[50:51]
	ds_bpermute_b32 v244, v226, v31
	ds_bpermute_b32 v245, v226, v33
	s_waitcnt lgkmcnt(0)
	v_cndmask_b32_e64 v231, v244, v245, s[50:51]
	ds_bpermute_b32 v244, v227, v26
	ds_bpermute_b32 v245, v227, v28
	s_waitcnt lgkmcnt(0)
	v_cndmask_b32_e64 v232, v244, v245, s[50:51]
	ds_bpermute_b32 v244, v227, v30
	ds_bpermute_b32 v245, v227, v32
	s_waitcnt lgkmcnt(0)
	v_cndmask_b32_e64 v233, v244, v245, s[50:51]
	ds_bpermute_b32 v244, v227, v27
	ds_bpermute_b32 v245, v227, v29
	s_waitcnt lgkmcnt(0)
	v_cndmask_b32_e64 v234, v244, v245, s[50:51]
	ds_bpermute_b32 v244, v227, v31
	ds_bpermute_b32 v245, v227, v33
	s_waitcnt lgkmcnt(0)
	v_cndmask_b32_e64 v235, v244, v245, s[50:51]
	v_mov_b32_e32 v26, v228
	v_mov_b32_e32 v27, v229
	v_mov_b32_e32 v28, v230
	v_mov_b32_e32 v29, v231
	v_mov_b32_e32 v30, v232
	v_mov_b32_e32 v31, v233
	v_mov_b32_e32 v32, v234
	v_mov_b32_e32 v33, v235
	ds_bpermute_b32 v244, v226, v34
	ds_bpermute_b32 v245, v226, v36
	s_waitcnt lgkmcnt(0)
	v_cndmask_b32_e64 v228, v244, v245, s[50:51]
	ds_bpermute_b32 v244, v226, v38
	ds_bpermute_b32 v245, v226, v40
	s_waitcnt lgkmcnt(0)
	v_cndmask_b32_e64 v229, v244, v245, s[50:51]
	ds_bpermute_b32 v244, v226, v35
	ds_bpermute_b32 v245, v226, v37
	s_waitcnt lgkmcnt(0)
	v_cndmask_b32_e64 v230, v244, v245, s[50:51]
	ds_bpermute_b32 v244, v226, v39
	ds_bpermute_b32 v245, v226, v41
	s_waitcnt lgkmcnt(0)
	v_cndmask_b32_e64 v231, v244, v245, s[50:51]
	ds_bpermute_b32 v244, v227, v34
	ds_bpermute_b32 v245, v227, v36
	s_waitcnt lgkmcnt(0)
	v_cndmask_b32_e64 v232, v244, v245, s[50:51]
	ds_bpermute_b32 v244, v227, v38
	ds_bpermute_b32 v245, v227, v40
	s_waitcnt lgkmcnt(0)
	v_cndmask_b32_e64 v233, v244, v245, s[50:51]
	ds_bpermute_b32 v244, v227, v35
	ds_bpermute_b32 v245, v227, v37
	s_waitcnt lgkmcnt(0)
	v_cndmask_b32_e64 v234, v244, v245, s[50:51]
	ds_bpermute_b32 v244, v227, v39
	ds_bpermute_b32 v245, v227, v41
	s_waitcnt lgkmcnt(0)
	v_cndmask_b32_e64 v235, v244, v245, s[50:51]
	v_mov_b32_e32 v34, v228
	v_mov_b32_e32 v35, v229
	v_mov_b32_e32 v36, v230
	v_mov_b32_e32 v37, v231
	v_mov_b32_e32 v38, v232
	v_mov_b32_e32 v39, v233
	v_mov_b32_e32 v40, v234
	v_mov_b32_e32 v41, v235
	ds_bpermute_b32 v244, v226, v42
	ds_bpermute_b32 v245, v226, v44
	s_waitcnt lgkmcnt(0)
	v_cndmask_b32_e64 v228, v244, v245, s[50:51]
	ds_bpermute_b32 v244, v226, v46
	ds_bpermute_b32 v245, v226, v48
	s_waitcnt lgkmcnt(0)
	v_cndmask_b32_e64 v229, v244, v245, s[50:51]
	ds_bpermute_b32 v244, v226, v43
	ds_bpermute_b32 v245, v226, v45
	s_waitcnt lgkmcnt(0)
	v_cndmask_b32_e64 v230, v244, v245, s[50:51]
	ds_bpermute_b32 v244, v226, v47
	ds_bpermute_b32 v245, v226, v49
	s_waitcnt lgkmcnt(0)
	v_cndmask_b32_e64 v231, v244, v245, s[50:51]
	ds_bpermute_b32 v244, v227, v42
	ds_bpermute_b32 v245, v227, v44
	s_waitcnt lgkmcnt(0)
	v_cndmask_b32_e64 v232, v244, v245, s[50:51]
	ds_bpermute_b32 v244, v227, v46
	ds_bpermute_b32 v245, v227, v48
	s_waitcnt lgkmcnt(0)
	v_cndmask_b32_e64 v233, v244, v245, s[50:51]
	ds_bpermute_b32 v244, v227, v43
	ds_bpermute_b32 v245, v227, v45
	s_waitcnt lgkmcnt(0)
	v_cndmask_b32_e64 v234, v244, v245, s[50:51]
	ds_bpermute_b32 v244, v227, v47
	ds_bpermute_b32 v245, v227, v49
	s_waitcnt lgkmcnt(0)
	v_cndmask_b32_e64 v235, v244, v245, s[50:51]
	v_mov_b32_e32 v42, v228
	v_mov_b32_e32 v43, v229
	v_mov_b32_e32 v44, v230
	v_mov_b32_e32 v45, v231
	v_mov_b32_e32 v46, v232
	v_mov_b32_e32 v47, v233
	v_mov_b32_e32 v48, v234
	v_mov_b32_e32 v49, v235
	ds_bpermute_b32 v244, v226, v50
	ds_bpermute_b32 v245, v226, v52
	s_waitcnt lgkmcnt(0)
	v_cndmask_b32_e64 v228, v244, v245, s[50:51]
	ds_bpermute_b32 v244, v226, v54
	ds_bpermute_b32 v245, v226, v56
	s_waitcnt lgkmcnt(0)
	v_cndmask_b32_e64 v229, v244, v245, s[50:51]
	ds_bpermute_b32 v244, v226, v51
	ds_bpermute_b32 v245, v226, v53
	s_waitcnt lgkmcnt(0)
	v_cndmask_b32_e64 v230, v244, v245, s[50:51]
	ds_bpermute_b32 v244, v226, v55
	ds_bpermute_b32 v245, v226, v57
	s_waitcnt lgkmcnt(0)
	v_cndmask_b32_e64 v231, v244, v245, s[50:51]
	ds_bpermute_b32 v244, v227, v50
	ds_bpermute_b32 v245, v227, v52
	s_waitcnt lgkmcnt(0)
	v_cndmask_b32_e64 v232, v244, v245, s[50:51]
	ds_bpermute_b32 v244, v227, v54
	ds_bpermute_b32 v245, v227, v56
	s_waitcnt lgkmcnt(0)
	v_cndmask_b32_e64 v233, v244, v245, s[50:51]
	ds_bpermute_b32 v244, v227, v51
	ds_bpermute_b32 v245, v227, v53
	s_waitcnt lgkmcnt(0)
	v_cndmask_b32_e64 v234, v244, v245, s[50:51]
	ds_bpermute_b32 v244, v227, v55
	ds_bpermute_b32 v245, v227, v57
	s_waitcnt lgkmcnt(0)
	v_cndmask_b32_e64 v235, v244, v245, s[50:51]
	v_mov_b32_e32 v50, v228
	v_mov_b32_e32 v51, v229
	v_mov_b32_e32 v52, v230
	v_mov_b32_e32 v53, v231
	v_mov_b32_e32 v54, v232
	v_mov_b32_e32 v55, v233
	v_mov_b32_e32 v56, v234
	v_mov_b32_e32 v57, v235
	ds_bpermute_b32 v244, v226, v58
	ds_bpermute_b32 v245, v226, v60
	s_waitcnt lgkmcnt(0)
	v_cndmask_b32_e64 v228, v244, v245, s[50:51]
	ds_bpermute_b32 v244, v226, v62
	ds_bpermute_b32 v245, v226, v64
	s_waitcnt lgkmcnt(0)
	v_cndmask_b32_e64 v229, v244, v245, s[50:51]
	ds_bpermute_b32 v244, v226, v59
	ds_bpermute_b32 v245, v226, v61
	s_waitcnt lgkmcnt(0)
	v_cndmask_b32_e64 v230, v244, v245, s[50:51]
	ds_bpermute_b32 v244, v226, v63
	ds_bpermute_b32 v245, v226, v65
	s_waitcnt lgkmcnt(0)
	v_cndmask_b32_e64 v231, v244, v245, s[50:51]
	ds_bpermute_b32 v244, v227, v58
	ds_bpermute_b32 v245, v227, v60
	s_waitcnt lgkmcnt(0)
	v_cndmask_b32_e64 v232, v244, v245, s[50:51]
	ds_bpermute_b32 v244, v227, v62
	ds_bpermute_b32 v245, v227, v64
	s_waitcnt lgkmcnt(0)
	v_cndmask_b32_e64 v233, v244, v245, s[50:51]
	ds_bpermute_b32 v244, v227, v59
	ds_bpermute_b32 v245, v227, v61
	s_waitcnt lgkmcnt(0)
	v_cndmask_b32_e64 v234, v244, v245, s[50:51]
	ds_bpermute_b32 v244, v227, v63
	ds_bpermute_b32 v245, v227, v65
	s_waitcnt lgkmcnt(0)
	v_cndmask_b32_e64 v235, v244, v245, s[50:51]
	v_mov_b32_e32 v58, v228
	v_mov_b32_e32 v59, v229
	v_mov_b32_e32 v60, v230
	v_mov_b32_e32 v61, v231
	v_mov_b32_e32 v62, v232
	v_mov_b32_e32 v63, v233
	v_mov_b32_e32 v64, v234
	v_mov_b32_e32 v65, v235
	ds_bpermute_b32 v244, v226, v66
	ds_bpermute_b32 v245, v226, v68
	s_waitcnt lgkmcnt(0)
	v_cndmask_b32_e64 v228, v244, v245, s[50:51]
	ds_bpermute_b32 v244, v226, v70
	ds_bpermute_b32 v245, v226, v72
	s_waitcnt lgkmcnt(0)
	v_cndmask_b32_e64 v229, v244, v245, s[50:51]
	ds_bpermute_b32 v244, v226, v67
	ds_bpermute_b32 v245, v226, v69
	s_waitcnt lgkmcnt(0)
	v_cndmask_b32_e64 v230, v244, v245, s[50:51]
	ds_bpermute_b32 v244, v226, v71
	ds_bpermute_b32 v245, v226, v73
	s_waitcnt lgkmcnt(0)
	v_cndmask_b32_e64 v231, v244, v245, s[50:51]
	ds_bpermute_b32 v244, v227, v66
	ds_bpermute_b32 v245, v227, v68
	s_waitcnt lgkmcnt(0)
	v_cndmask_b32_e64 v232, v244, v245, s[50:51]
	ds_bpermute_b32 v244, v227, v70
	ds_bpermute_b32 v245, v227, v72
	s_waitcnt lgkmcnt(0)
	v_cndmask_b32_e64 v233, v244, v245, s[50:51]
	ds_bpermute_b32 v244, v227, v67
	ds_bpermute_b32 v245, v227, v69
	s_waitcnt lgkmcnt(0)
	v_cndmask_b32_e64 v234, v244, v245, s[50:51]
	ds_bpermute_b32 v244, v227, v71
	ds_bpermute_b32 v245, v227, v73
	s_waitcnt lgkmcnt(0)
	v_cndmask_b32_e64 v235, v244, v245, s[50:51]
	v_mov_b32_e32 v66, v228
	v_mov_b32_e32 v67, v229
	v_mov_b32_e32 v68, v230
	v_mov_b32_e32 v69, v231
	v_mov_b32_e32 v70, v232
	v_mov_b32_e32 v71, v233
	v_mov_b32_e32 v72, v234
	v_mov_b32_e32 v73, v235
	ds_bpermute_b32 v244, v226, v74
	ds_bpermute_b32 v245, v226, v76
	s_waitcnt lgkmcnt(0)
	v_cndmask_b32_e64 v228, v244, v245, s[50:51]
	ds_bpermute_b32 v244, v226, v78
	ds_bpermute_b32 v245, v226, v80
	s_waitcnt lgkmcnt(0)
	v_cndmask_b32_e64 v229, v244, v245, s[50:51]
	ds_bpermute_b32 v244, v226, v75
	ds_bpermute_b32 v245, v226, v77
	s_waitcnt lgkmcnt(0)
	v_cndmask_b32_e64 v230, v244, v245, s[50:51]
	ds_bpermute_b32 v244, v226, v79
	ds_bpermute_b32 v245, v226, v81
	s_waitcnt lgkmcnt(0)
	v_cndmask_b32_e64 v231, v244, v245, s[50:51]
	ds_bpermute_b32 v244, v227, v74
	ds_bpermute_b32 v245, v227, v76
	s_waitcnt lgkmcnt(0)
	v_cndmask_b32_e64 v232, v244, v245, s[50:51]
	ds_bpermute_b32 v244, v227, v78
	ds_bpermute_b32 v245, v227, v80
	s_waitcnt lgkmcnt(0)
	v_cndmask_b32_e64 v233, v244, v245, s[50:51]
	ds_bpermute_b32 v244, v227, v75
	ds_bpermute_b32 v245, v227, v77
	s_waitcnt lgkmcnt(0)
	v_cndmask_b32_e64 v234, v244, v245, s[50:51]
	ds_bpermute_b32 v244, v227, v79
	ds_bpermute_b32 v245, v227, v81
	s_waitcnt lgkmcnt(0)
	v_cndmask_b32_e64 v235, v244, v245, s[50:51]
	v_mov_b32_e32 v74, v228
	v_mov_b32_e32 v75, v229
	v_mov_b32_e32 v76, v230
	v_mov_b32_e32 v77, v231
	v_mov_b32_e32 v78, v232
	v_mov_b32_e32 v79, v233
	v_mov_b32_e32 v80, v234
	v_mov_b32_e32 v81, v235
	ds_bpermute_b32 v244, v226, v82
	ds_bpermute_b32 v245, v226, v84
	s_waitcnt lgkmcnt(0)
	v_cndmask_b32_e64 v228, v244, v245, s[50:51]
	ds_bpermute_b32 v244, v226, v86
	ds_bpermute_b32 v245, v226, v88
	s_waitcnt lgkmcnt(0)
	v_cndmask_b32_e64 v229, v244, v245, s[50:51]
	ds_bpermute_b32 v244, v226, v83
	ds_bpermute_b32 v245, v226, v85
	s_waitcnt lgkmcnt(0)
	v_cndmask_b32_e64 v230, v244, v245, s[50:51]
	ds_bpermute_b32 v244, v226, v87
	ds_bpermute_b32 v245, v226, v89
	s_waitcnt lgkmcnt(0)
	v_cndmask_b32_e64 v231, v244, v245, s[50:51]
	ds_bpermute_b32 v244, v227, v82
	ds_bpermute_b32 v245, v227, v84
	s_waitcnt lgkmcnt(0)
	v_cndmask_b32_e64 v232, v244, v245, s[50:51]
	ds_bpermute_b32 v244, v227, v86
	ds_bpermute_b32 v245, v227, v88
	s_waitcnt lgkmcnt(0)
	v_cndmask_b32_e64 v233, v244, v245, s[50:51]
	ds_bpermute_b32 v244, v227, v83
	ds_bpermute_b32 v245, v227, v85
	s_waitcnt lgkmcnt(0)
	v_cndmask_b32_e64 v234, v244, v245, s[50:51]
	ds_bpermute_b32 v244, v227, v87
	ds_bpermute_b32 v245, v227, v89
	s_waitcnt lgkmcnt(0)
	v_cndmask_b32_e64 v235, v244, v245, s[50:51]
	v_mov_b32_e32 v82, v228
	v_mov_b32_e32 v83, v229
	v_mov_b32_e32 v84, v230
	v_mov_b32_e32 v85, v231
	v_mov_b32_e32 v86, v232
	v_mov_b32_e32 v87, v233
	v_mov_b32_e32 v88, v234
	v_mov_b32_e32 v89, v235
	ds_bpermute_b32 v244, v226, v90
	ds_bpermute_b32 v245, v226, v92
	s_waitcnt lgkmcnt(0)
	v_cndmask_b32_e64 v228, v244, v245, s[50:51]
	ds_bpermute_b32 v244, v226, v94
	ds_bpermute_b32 v245, v226, v96
	s_waitcnt lgkmcnt(0)
	v_cndmask_b32_e64 v229, v244, v245, s[50:51]
	ds_bpermute_b32 v244, v226, v91
	ds_bpermute_b32 v245, v226, v93
	s_waitcnt lgkmcnt(0)
	v_cndmask_b32_e64 v230, v244, v245, s[50:51]
	ds_bpermute_b32 v244, v226, v95
	ds_bpermute_b32 v245, v226, v97
	s_waitcnt lgkmcnt(0)
	v_cndmask_b32_e64 v231, v244, v245, s[50:51]
	ds_bpermute_b32 v244, v227, v90
	ds_bpermute_b32 v245, v227, v92
	s_waitcnt lgkmcnt(0)
	v_cndmask_b32_e64 v232, v244, v245, s[50:51]
	ds_bpermute_b32 v244, v227, v94
	ds_bpermute_b32 v245, v227, v96
	s_waitcnt lgkmcnt(0)
	v_cndmask_b32_e64 v233, v244, v245, s[50:51]
	ds_bpermute_b32 v244, v227, v91
	ds_bpermute_b32 v245, v227, v93
	s_waitcnt lgkmcnt(0)
	v_cndmask_b32_e64 v234, v244, v245, s[50:51]
	ds_bpermute_b32 v244, v227, v95
	ds_bpermute_b32 v245, v227, v97
	s_waitcnt lgkmcnt(0)
	v_cndmask_b32_e64 v235, v244, v245, s[50:51]
	v_mov_b32_e32 v90, v228
	v_mov_b32_e32 v91, v229
	v_mov_b32_e32 v92, v230
	v_mov_b32_e32 v93, v231
	v_mov_b32_e32 v94, v232
	v_mov_b32_e32 v95, v233
	v_mov_b32_e32 v96, v234
	v_mov_b32_e32 v97, v235
	ds_bpermute_b32 v244, v226, v98
	ds_bpermute_b32 v245, v226, v100
	s_waitcnt lgkmcnt(0)
	v_cndmask_b32_e64 v228, v244, v245, s[50:51]
	ds_bpermute_b32 v244, v226, v102
	ds_bpermute_b32 v245, v226, v104
	s_waitcnt lgkmcnt(0)
	v_cndmask_b32_e64 v229, v244, v245, s[50:51]
	ds_bpermute_b32 v244, v226, v99
	ds_bpermute_b32 v245, v226, v101
	s_waitcnt lgkmcnt(0)
	v_cndmask_b32_e64 v230, v244, v245, s[50:51]
	ds_bpermute_b32 v244, v226, v103
	ds_bpermute_b32 v245, v226, v105
	s_waitcnt lgkmcnt(0)
	v_cndmask_b32_e64 v231, v244, v245, s[50:51]
	ds_bpermute_b32 v244, v227, v98
	ds_bpermute_b32 v245, v227, v100
	s_waitcnt lgkmcnt(0)
	v_cndmask_b32_e64 v232, v244, v245, s[50:51]
	ds_bpermute_b32 v244, v227, v102
	ds_bpermute_b32 v245, v227, v104
	s_waitcnt lgkmcnt(0)
	v_cndmask_b32_e64 v233, v244, v245, s[50:51]
	ds_bpermute_b32 v244, v227, v99
	ds_bpermute_b32 v245, v227, v101
	s_waitcnt lgkmcnt(0)
	v_cndmask_b32_e64 v234, v244, v245, s[50:51]
	ds_bpermute_b32 v244, v227, v103
	ds_bpermute_b32 v245, v227, v105
	s_waitcnt lgkmcnt(0)
	v_cndmask_b32_e64 v235, v244, v245, s[50:51]
	v_mov_b32_e32 v98, v228
	v_mov_b32_e32 v99, v229
	v_mov_b32_e32 v100, v230
	v_mov_b32_e32 v101, v231
	v_mov_b32_e32 v102, v232
	v_mov_b32_e32 v103, v233
	v_mov_b32_e32 v104, v234
	v_mov_b32_e32 v105, v235
	.p2align 6
.LBB0_21:
	v_exp_f32_e64 v156, -|v154|
	v_max_f32 v157, 0, v154
	v_add_f32 v156, 1.0, v156
	v_log_f32 v156, v156
	s_nop 0
	v_fma_mixlo_f16 v155, v156, 1.0, v157
	ds_write_b16 v148, v155
	v_mov_b32_e32 v192, v106
	v_mov_b32_e32 v193, 0
	v_mov_b32_e32 v196, v110
	v_mov_b32_e32 v197, 0
	v_mul_f32 v182, -2.0, v153
	s_waitcnt lgkmcnt(0)
	s_barrier
	ds_read_b128 v[216:219], v139
	s_nop 2
	ds_read_b128 v[220:223], v141
	s_waitcnt lgkmcnt(1)
	v_smfmac_f32_16x16x64_f16 v[192:195], v[216:219], v[6:13], v191
	v_smfmac_f32_16x16x64_f16 v[196:199], v[216:219], v[26:33], v191
	s_waitcnt lgkmcnt(0)
	v_smfmac_f32_16x16x64_f16 v[192:195], v[220:223], v[14:21], v191
	v_smfmac_f32_16x16x64_f16 v[196:199], v[220:223], v[34:41], v191
	s_nop 6
	v_add_f32_e32 v224, v192, v193
	v_add_f32_e32 v225, v196, v197
	v_cndmask_b32_e64 v154, v224, v225, s[0:1]
	v_exp_f32_e64 v156, -|v154|
	v_max_f32 v157, 0, v154
	v_add_f32 v156, 1.0, v156
	v_log_f32 v156, v156
	s_nop 0
	v_fma_mixlo_f16 v155, v156, 1.0, v157
	ds_write_b16 v149, v155
	v_mov_b32_e32 v200, v114
	v_mov_b32_e32 v201, 0
	v_mov_b32_e32 v204, v118
	v_mov_b32_e32 v205, 0
	v_mov_b32_e32 v208, v122
	v_mov_b32_e32 v209, 0
	v_mov_b32_e32 v212, v126
	v_mov_b32_e32 v213, 0
	s_waitcnt lgkmcnt(0)
	s_barrier
	ds_read_b128 v[216:219], v143
	s_nop 2
	ds_read_b128 v[220:223], v145
	s_waitcnt lgkmcnt(1)
	v_smfmac_f32_16x16x64_f16 v[200:203], v[216:219], v[42:49], v191
	v_smfmac_f32_16x16x64_f16 v[204:207], v[216:219], v[58:65], v191
	v_smfmac_f32_16x16x64_f16 v[208:211], v[216:219], v[74:81], v191
	v_smfmac_f32_16x16x64_f16 v[212:215], v[216:219], v[90:97], v191
	s_waitcnt lgkmcnt(0)
	v_smfmac_f32_16x16x64_f16 v[200:203], v[220:223], v[50:57], v191
	v_smfmac_f32_16x16x64_f16 v[204:207], v[220:223], v[66:73], v191
	v_smfmac_f32_16x16x64_f16 v[208:211], v[220:223], v[82:89], v191
	v_smfmac_f32_16x16x64_f16 v[212:215], v[220:223], v[98:105], v191
	s_nop 4
	v_add_f32_e32 v224, v200, v201
	v_add_f32_e32 v225, v204, v205
	v_add_f32_e32 v226, v208, v209
	v_add_f32_e32 v227, v212, v213
	v_cndmask_b32_e64 v170, v225, v224, s[6:7]
	v_cndmask_b32_e64 v170, v170, v226, s[0:1]
	v_cndmask_b32_e64 v170, v170, v227, s[4:5]
	v_exp_f32_e32 v170, v170
	s_nop 0
	v_add_f32_e32 v170, 1.0, v170
	v_rcp_f32_e32 v170, v170
	s_nop 0
	v_fmac_f32_e32 v153, v170, v182
	s_nop 1
	v_add_f32_dpp v153, v153, v153 quad_perm:[1,0,3,2] row_mask:0xf bank_mask:0xf bound_ctrl:1
	s_nop 1
	v_add_f32_dpp v153, v153, v153 quad_perm:[2,3,0,1] row_mask:0xf bank_mask:0xf bound_ctrl:1
	s_nop 1
	v_add_f32_dpp v153, v153, v153 row_half_mirror row_mask:0xf bank_mask:0xf bound_ctrl:1
	v_cvt_f16_f32_e32 v170, v153
	ds_write_b16 v150, v170
	s_waitcnt lgkmcnt(0)
	s_barrier
	ds_read_b128 v[154:157], v147
	s_waitcnt lgkmcnt(0)
	v_mfma_f32_16x16x32_f16 v[130:133], v[154:157], v[2:5], v[130:133]
	v_mfma_f32_16x16x32_f16 v[154:157], v[154:157], v[22:25], v[134:137]
	s_nop 2
	v_add_u32_e32 v134, s3, v151
	ds_read_b32 v135, v134
	s_nop 2
	v_cndmask_b32_e64 v136, v130, v154, s[0:1]
	v_exp_f32_e64 v158, -|v136|
	v_max_f32 v159, 0, v136
	v_add_f32 v158, 1.0, v158
	v_log_f32 v158, v158
	s_nop 0
	v_fma_mixlo_f16 v137, v158, 1.0, v159
	ds_write_b16 v148, v137
	v_mov_b32_e32 v192, v106
	v_mov_b32_e32 v193, 0
	v_mov_b32_e32 v196, v110
	v_mov_b32_e32 v197, 0
	v_add_f32_e32 v136, v152, v153
	v_mul_f32 v137, -2.0, v135
	s_waitcnt lgkmcnt(0)
	s_barrier
	ds_read_b128 v[216:219], v139
	s_nop 2
	ds_read_b128 v[220:223], v141
	s_waitcnt lgkmcnt(1)
	v_smfmac_f32_16x16x64_f16 v[192:195], v[216:219], v[6:13], v191
	v_smfmac_f32_16x16x64_f16 v[196:199], v[216:219], v[26:33], v191
	s_waitcnt lgkmcnt(0)
	v_smfmac_f32_16x16x64_f16 v[192:195], v[220:223], v[14:21], v191
	v_smfmac_f32_16x16x64_f16 v[196:199], v[220:223], v[34:41], v191
	s_nop 6
	v_add_f32_e32 v224, v192, v193
	v_add_f32_e32 v225, v196, v197
	v_cndmask_b32_e64 v152, v224, v225, s[0:1]
	v_exp_f32_e64 v158, -|v152|
	v_max_f32 v159, 0, v152
	v_add_f32 v158, 1.0, v158
	v_log_f32 v158, v158
	s_nop 0
	v_fma_mixlo_f16 v153, v158, 1.0, v159
	ds_write_b16 v149, v153
	v_mov_b32_e32 v200, v114
	v_mov_b32_e32 v201, 0
	v_mov_b32_e32 v204, v118
	v_mov_b32_e32 v205, 0
	v_mov_b32_e32 v208, v122
	v_mov_b32_e32 v209, 0
	v_mov_b32_e32 v212, v126
	v_mov_b32_e32 v213, 0
	s_waitcnt lgkmcnt(0)
	s_barrier
	ds_read_b128 v[216:219], v143
	s_nop 2
	ds_read_b128 v[220:223], v145
	s_waitcnt lgkmcnt(1)
	v_smfmac_f32_16x16x64_f16 v[200:203], v[216:219], v[42:49], v191
	v_smfmac_f32_16x16x64_f16 v[204:207], v[216:219], v[58:65], v191
	v_smfmac_f32_16x16x64_f16 v[208:211], v[216:219], v[74:81], v191
	v_smfmac_f32_16x16x64_f16 v[212:215], v[216:219], v[90:97], v191
	s_waitcnt lgkmcnt(0)
	v_smfmac_f32_16x16x64_f16 v[200:203], v[220:223], v[50:57], v191
	v_smfmac_f32_16x16x64_f16 v[204:207], v[220:223], v[66:73], v191
	v_smfmac_f32_16x16x64_f16 v[208:211], v[220:223], v[82:89], v191
	v_smfmac_f32_16x16x64_f16 v[212:215], v[220:223], v[98:105], v191
	s_nop 4
	v_add_f32_e32 v224, v200, v201
	v_add_f32_e32 v225, v204, v205
	v_add_f32_e32 v226, v208, v209
	v_add_f32_e32 v227, v212, v213
	v_cndmask_b32_e64 v152, v225, v224, s[6:7]
	v_cndmask_b32_e64 v152, v152, v226, s[0:1]
	v_cndmask_b32_e64 v152, v152, v227, s[4:5]
	v_exp_f32_e32 v152, v152
	s_nop 0
	v_add_f32_e32 v152, 1.0, v152
	v_rcp_f32_e32 v152, v152
	s_nop 0
	v_fmac_f32_e32 v135, v152, v137
	s_nop 1
	v_add_f32_dpp v135, v135, v135 quad_perm:[1,0,3,2] row_mask:0xf bank_mask:0xf bound_ctrl:1
	s_nop 1
	v_add_f32_dpp v135, v135, v135 quad_perm:[2,3,0,1] row_mask:0xf bank_mask:0xf bound_ctrl:1
	s_nop 1
	v_add_f32_dpp v135, v135, v135 row_half_mirror row_mask:0xf bank_mask:0xf bound_ctrl:1
	v_cvt_f16_f32_e32 v137, v135
	ds_write_b16 v150, v137
	s_waitcnt lgkmcnt(0)
	s_barrier
	ds_read_b128 v[158:161], v147
	ds_read_b32 v137, v134 offset:32
	v_add_f32_e32 v135, v136, v135
	s_waitcnt lgkmcnt(1)
	v_mfma_f32_16x16x32_f16 v[130:133], v[158:161], v[2:5], v[130:133]
	v_mfma_f32_16x16x32_f16 v[152:155], v[158:161], v[22:25], v[154:157]
	s_nop 7
	v_cndmask_b32_e64 v156, v130, v152, s[0:1]
	v_exp_f32_e64 v158, -|v156|
	v_max_f32 v159, 0, v156
	v_add_f32 v158, 1.0, v158
	v_log_f32 v158, v158
	s_nop 0
	v_fma_mixlo_f16 v157, v158, 1.0, v159
	ds_write_b16 v148, v157
	v_mov_b32_e32 v192, v106
	v_mov_b32_e32 v193, 0
	v_mov_b32_e32 v196, v110
	v_mov_b32_e32 v197, 0
	v_mul_f32 v136, -2.0, v137
	s_waitcnt lgkmcnt(0)
	s_barrier
	ds_read_b128 v[216:219], v139
	s_nop 2
	ds_read_b128 v[220:223], v141
	s_waitcnt lgkmcnt(1)
	v_smfmac_f32_16x16x64_f16 v[192:195], v[216:219], v[6:13], v191
	v_smfmac_f32_16x16x64_f16 v[196:199], v[216:219], v[26:33], v191
	s_waitcnt lgkmcnt(0)
	v_smfmac_f32_16x16x64_f16 v[192:195], v[220:223], v[14:21], v191
	v_smfmac_f32_16x16x64_f16 v[196:199], v[220:223], v[34:41], v191
	s_nop 6
	v_add_f32_e32 v224, v192, v193
	v_add_f32_e32 v225, v196, v197
	v_cndmask_b32_e64 v156, v224, v225, s[0:1]
	v_exp_f32_e64 v158, -|v156|
	v_max_f32 v159, 0, v156
	v_add_f32 v158, 1.0, v158
	v_log_f32 v158, v158
	s_nop 0
	v_fma_mixlo_f16 v157, v158, 1.0, v159
	ds_write_b16 v149, v157
	v_mov_b32_e32 v200, v114
	v_mov_b32_e32 v201, 0
	v_mov_b32_e32 v204, v118
	v_mov_b32_e32 v205, 0
	v_mov_b32_e32 v208, v122
	v_mov_b32_e32 v209, 0
	v_mov_b32_e32 v212, v126
	v_mov_b32_e32 v213, 0
	s_waitcnt lgkmcnt(0)
	s_barrier
	ds_read_b128 v[216:219], v143
	s_nop 2
	ds_read_b128 v[220:223], v145
	s_waitcnt lgkmcnt(1)
	v_smfmac_f32_16x16x64_f16 v[200:203], v[216:219], v[42:49], v191
	v_smfmac_f32_16x16x64_f16 v[204:207], v[216:219], v[58:65], v191
	v_smfmac_f32_16x16x64_f16 v[208:211], v[216:219], v[74:81], v191
	v_smfmac_f32_16x16x64_f16 v[212:215], v[216:219], v[90:97], v191
	s_waitcnt lgkmcnt(0)
	v_smfmac_f32_16x16x64_f16 v[200:203], v[220:223], v[50:57], v191
	v_smfmac_f32_16x16x64_f16 v[204:207], v[220:223], v[66:73], v191
	v_smfmac_f32_16x16x64_f16 v[208:211], v[220:223], v[82:89], v191
	v_smfmac_f32_16x16x64_f16 v[212:215], v[220:223], v[98:105], v191
	s_nop 4
	v_add_f32_e32 v224, v200, v201
	v_add_f32_e32 v225, v204, v205
	v_add_f32_e32 v226, v208, v209
	v_add_f32_e32 v227, v212, v213
	v_cndmask_b32_e64 v172, v225, v224, s[6:7]
	v_cndmask_b32_e64 v172, v172, v226, s[0:1]
	v_cndmask_b32_e64 v172, v172, v227, s[4:5]
	v_exp_f32_e32 v172, v172
	s_nop 0
	v_add_f32_e32 v172, 1.0, v172
	v_rcp_f32_e32 v172, v172
	s_nop 0
	v_fmac_f32_e32 v137, v172, v136
	s_nop 1
	v_add_f32_dpp v136, v137, v137 quad_perm:[1,0,3,2] row_mask:0xf bank_mask:0xf bound_ctrl:1
	s_nop 1
	v_add_f32_dpp v136, v136, v136 quad_perm:[2,3,0,1] row_mask:0xf bank_mask:0xf bound_ctrl:1
	s_nop 1
	v_add_f32_dpp v136, v136, v136 row_half_mirror row_mask:0xf bank_mask:0xf bound_ctrl:1
	v_cvt_f16_f32_e32 v137, v136
	ds_write_b16 v150, v137
	s_waitcnt lgkmcnt(0)
	s_barrier
	ds_read_b128 v[156:159], v147
	ds_read_b32 v137, v134 offset:64
	v_add_f32_e32 v135, v135, v136
	s_waitcnt lgkmcnt(1)
	v_mfma_f32_16x16x32_f16 v[130:133], v[156:159], v[2:5], v[130:133]
	v_mfma_f32_16x16x32_f16 v[152:155], v[156:159], v[22:25], v[152:155]
	s_nop 7
	v_cndmask_b32_e64 v156, v130, v152, s[0:1]
	v_exp_f32_e64 v158, -|v156|
	v_max_f32 v159, 0, v156
	v_add_f32 v158, 1.0, v158
	v_log_f32 v158, v158
	s_nop 0
	v_fma_mixlo_f16 v157, v158, 1.0, v159
	ds_write_b16 v148, v157
	v_mov_b32_e32 v192, v106
	v_mov_b32_e32 v193, 0
	v_mov_b32_e32 v196, v110
	v_mov_b32_e32 v197, 0
	v_mul_f32 v136, -2.0, v137
	s_waitcnt lgkmcnt(0)
	s_barrier
	ds_read_b128 v[216:219], v139
	s_nop 2
	ds_read_b128 v[220:223], v141
	s_waitcnt lgkmcnt(1)
	v_smfmac_f32_16x16x64_f16 v[192:195], v[216:219], v[6:13], v191
	v_smfmac_f32_16x16x64_f16 v[196:199], v[216:219], v[26:33], v191
	s_waitcnt lgkmcnt(0)
	v_smfmac_f32_16x16x64_f16 v[192:195], v[220:223], v[14:21], v191
	v_smfmac_f32_16x16x64_f16 v[196:199], v[220:223], v[34:41], v191
	s_nop 6
	v_add_f32_e32 v224, v192, v193
	v_add_f32_e32 v225, v196, v197
	v_cndmask_b32_e64 v156, v224, v225, s[0:1]
	v_exp_f32_e64 v158, -|v156|
	v_max_f32 v159, 0, v156
	v_add_f32 v158, 1.0, v158
	v_log_f32 v158, v158
	s_nop 0
	v_fma_mixlo_f16 v157, v158, 1.0, v159
	ds_write_b16 v149, v157
	v_mov_b32_e32 v200, v114
	v_mov_b32_e32 v201, 0
	v_mov_b32_e32 v204, v118
	v_mov_b32_e32 v205, 0
	v_mov_b32_e32 v208, v122
	v_mov_b32_e32 v209, 0
	v_mov_b32_e32 v212, v126
	v_mov_b32_e32 v213, 0
	s_waitcnt lgkmcnt(0)
	s_barrier
	ds_read_b128 v[216:219], v143
	s_nop 2
	ds_read_b128 v[220:223], v145
	s_waitcnt lgkmcnt(1)
	v_smfmac_f32_16x16x64_f16 v[200:203], v[216:219], v[42:49], v191
	v_smfmac_f32_16x16x64_f16 v[204:207], v[216:219], v[58:65], v191
	v_smfmac_f32_16x16x64_f16 v[208:211], v[216:219], v[74:81], v191
	v_smfmac_f32_16x16x64_f16 v[212:215], v[216:219], v[90:97], v191
	s_waitcnt lgkmcnt(0)
	v_smfmac_f32_16x16x64_f16 v[200:203], v[220:223], v[50:57], v191
	v_smfmac_f32_16x16x64_f16 v[204:207], v[220:223], v[66:73], v191
	v_smfmac_f32_16x16x64_f16 v[208:211], v[220:223], v[82:89], v191
	v_smfmac_f32_16x16x64_f16 v[212:215], v[220:223], v[98:105], v191
	s_nop 4
	v_add_f32_e32 v224, v200, v201
	v_add_f32_e32 v225, v204, v205
	v_add_f32_e32 v226, v208, v209
	v_add_f32_e32 v227, v212, v213
	v_cndmask_b32_e64 v172, v225, v224, s[6:7]
	v_cndmask_b32_e64 v172, v172, v226, s[0:1]
	v_cndmask_b32_e64 v172, v172, v227, s[4:5]
	v_exp_f32_e32 v172, v172
	s_nop 0
	v_add_f32_e32 v172, 1.0, v172
	v_rcp_f32_e32 v172, v172
	s_nop 0
	v_fmac_f32_e32 v137, v172, v136
	s_nop 1
	v_add_f32_dpp v136, v137, v137 quad_perm:[1,0,3,2] row_mask:0xf bank_mask:0xf bound_ctrl:1
	s_nop 1
	v_add_f32_dpp v136, v136, v136 quad_perm:[2,3,0,1] row_mask:0xf bank_mask:0xf bound_ctrl:1
	s_nop 1
	v_add_f32_dpp v136, v136, v136 row_half_mirror row_mask:0xf bank_mask:0xf bound_ctrl:1
	v_cvt_f16_f32_e32 v137, v136
	ds_write_b16 v150, v137
	s_waitcnt lgkmcnt(0)
	s_barrier
	ds_read_b128 v[156:159], v147
	ds_read_b32 v137, v134 offset:96
	v_add_f32_e32 v135, v135, v136
	s_waitcnt lgkmcnt(1)
	v_mfma_f32_16x16x32_f16 v[130:133], v[156:159], v[2:5], v[130:133]
	v_mfma_f32_16x16x32_f16 v[152:155], v[156:159], v[22:25], v[152:155]
	s_nop 7
	v_cndmask_b32_e64 v156, v130, v152, s[0:1]
	v_exp_f32_e64 v158, -|v156|
	v_max_f32 v159, 0, v156
	v_add_f32 v158, 1.0, v158
	v_log_f32 v158, v158
	s_nop 0
	v_fma_mixlo_f16 v157, v158, 1.0, v159
	ds_write_b16 v148, v157
	v_mov_b32_e32 v192, v106
	v_mov_b32_e32 v193, 0
	v_mov_b32_e32 v196, v110
	v_mov_b32_e32 v197, 0
	v_mul_f32 v136, -2.0, v137
	s_waitcnt lgkmcnt(0)
	s_barrier
	ds_read_b128 v[216:219], v139
	s_nop 2
	ds_read_b128 v[220:223], v141
	s_waitcnt lgkmcnt(1)
	v_smfmac_f32_16x16x64_f16 v[192:195], v[216:219], v[6:13], v191
	v_smfmac_f32_16x16x64_f16 v[196:199], v[216:219], v[26:33], v191
	s_waitcnt lgkmcnt(0)
	v_smfmac_f32_16x16x64_f16 v[192:195], v[220:223], v[14:21], v191
	v_smfmac_f32_16x16x64_f16 v[196:199], v[220:223], v[34:41], v191
	s_nop 6
	v_add_f32_e32 v224, v192, v193
	v_add_f32_e32 v225, v196, v197
	v_cndmask_b32_e64 v156, v224, v225, s[0:1]
	v_exp_f32_e64 v158, -|v156|
	v_max_f32 v159, 0, v156
	v_add_f32 v158, 1.0, v158
	v_log_f32 v158, v158
	s_nop 0
	v_fma_mixlo_f16 v157, v158, 1.0, v159
	ds_write_b16 v149, v157
	v_mov_b32_e32 v200, v114
	v_mov_b32_e32 v201, 0
	v_mov_b32_e32 v204, v118
	v_mov_b32_e32 v205, 0
	v_mov_b32_e32 v208, v122
	v_mov_b32_e32 v209, 0
	v_mov_b32_e32 v212, v126
	v_mov_b32_e32 v213, 0
	s_waitcnt lgkmcnt(0)
	s_barrier
	ds_read_b128 v[216:219], v143
	s_nop 2
	ds_read_b128 v[220:223], v145
	s_waitcnt lgkmcnt(1)
	v_smfmac_f32_16x16x64_f16 v[200:203], v[216:219], v[42:49], v191
	v_smfmac_f32_16x16x64_f16 v[204:207], v[216:219], v[58:65], v191
	v_smfmac_f32_16x16x64_f16 v[208:211], v[216:219], v[74:81], v191
	v_smfmac_f32_16x16x64_f16 v[212:215], v[216:219], v[90:97], v191
	s_waitcnt lgkmcnt(0)
	v_smfmac_f32_16x16x64_f16 v[200:203], v[220:223], v[50:57], v191
	v_smfmac_f32_16x16x64_f16 v[204:207], v[220:223], v[66:73], v191
	v_smfmac_f32_16x16x64_f16 v[208:211], v[220:223], v[82:89], v191
	v_smfmac_f32_16x16x64_f16 v[212:215], v[220:223], v[98:105], v191
	s_nop 4
	v_add_f32_e32 v224, v200, v201
	v_add_f32_e32 v225, v204, v205
	v_add_f32_e32 v226, v208, v209
	v_add_f32_e32 v227, v212, v213
	v_cndmask_b32_e64 v172, v225, v224, s[6:7]
	v_cndmask_b32_e64 v172, v172, v226, s[0:1]
	v_cndmask_b32_e64 v172, v172, v227, s[4:5]
	v_exp_f32_e32 v172, v172
	s_nop 0
	v_add_f32_e32 v172, 1.0, v172
	v_rcp_f32_e32 v172, v172
	s_nop 0
	v_fmac_f32_e32 v137, v172, v136
	s_nop 1
	v_add_f32_dpp v136, v137, v137 quad_perm:[1,0,3,2] row_mask:0xf bank_mask:0xf bound_ctrl:1
	s_nop 1
	v_add_f32_dpp v136, v136, v136 quad_perm:[2,3,0,1] row_mask:0xf bank_mask:0xf bound_ctrl:1
	s_nop 1
	v_add_f32_dpp v136, v136, v136 row_half_mirror row_mask:0xf bank_mask:0xf bound_ctrl:1
	v_cvt_f16_f32_e32 v137, v136
	ds_write_b16 v150, v137
	s_waitcnt lgkmcnt(0)
	s_barrier
	ds_read_b128 v[156:159], v147
	ds_read_b32 v137, v134 offset:128
	v_add_f32_e32 v135, v135, v136
	s_waitcnt lgkmcnt(1)
	v_mfma_f32_16x16x32_f16 v[130:133], v[156:159], v[2:5], v[130:133]
	v_mfma_f32_16x16x32_f16 v[152:155], v[156:159], v[22:25], v[152:155]
	s_nop 7
	v_cndmask_b32_e64 v156, v130, v152, s[0:1]
	v_exp_f32_e64 v158, -|v156|
	v_max_f32 v159, 0, v156
	v_add_f32 v158, 1.0, v158
	v_log_f32 v158, v158
	s_nop 0
	v_fma_mixlo_f16 v157, v158, 1.0, v159
	ds_write_b16 v148, v157
	v_mov_b32_e32 v192, v106
	v_mov_b32_e32 v193, 0
	v_mov_b32_e32 v196, v110
	v_mov_b32_e32 v197, 0
	v_mul_f32 v136, -2.0, v137
	s_waitcnt lgkmcnt(0)
	s_barrier
	ds_read_b128 v[216:219], v139
	s_nop 2
	ds_read_b128 v[220:223], v141
	s_waitcnt lgkmcnt(1)
	v_smfmac_f32_16x16x64_f16 v[192:195], v[216:219], v[6:13], v191
	v_smfmac_f32_16x16x64_f16 v[196:199], v[216:219], v[26:33], v191
	s_waitcnt lgkmcnt(0)
	v_smfmac_f32_16x16x64_f16 v[192:195], v[220:223], v[14:21], v191
	v_smfmac_f32_16x16x64_f16 v[196:199], v[220:223], v[34:41], v191
	s_nop 6
	v_add_f32_e32 v224, v192, v193
	v_add_f32_e32 v225, v196, v197
	v_cndmask_b32_e64 v156, v224, v225, s[0:1]
	v_exp_f32_e64 v158, -|v156|
	v_max_f32 v159, 0, v156
	v_add_f32 v158, 1.0, v158
	v_log_f32 v158, v158
	s_nop 0
	v_fma_mixlo_f16 v157, v158, 1.0, v159
	ds_write_b16 v149, v157
	v_mov_b32_e32 v200, v114
	v_mov_b32_e32 v201, 0
	v_mov_b32_e32 v204, v118
	v_mov_b32_e32 v205, 0
	v_mov_b32_e32 v208, v122
	v_mov_b32_e32 v209, 0
	v_mov_b32_e32 v212, v126
	v_mov_b32_e32 v213, 0
	s_waitcnt lgkmcnt(0)
	s_barrier
	ds_read_b128 v[216:219], v143
	s_nop 2
	ds_read_b128 v[220:223], v145
	s_waitcnt lgkmcnt(1)
	v_smfmac_f32_16x16x64_f16 v[200:203], v[216:219], v[42:49], v191
	v_smfmac_f32_16x16x64_f16 v[204:207], v[216:219], v[58:65], v191
	v_smfmac_f32_16x16x64_f16 v[208:211], v[216:219], v[74:81], v191
	v_smfmac_f32_16x16x64_f16 v[212:215], v[216:219], v[90:97], v191
	s_waitcnt lgkmcnt(0)
	v_smfmac_f32_16x16x64_f16 v[200:203], v[220:223], v[50:57], v191
	v_smfmac_f32_16x16x64_f16 v[204:207], v[220:223], v[66:73], v191
	v_smfmac_f32_16x16x64_f16 v[208:211], v[220:223], v[82:89], v191
	v_smfmac_f32_16x16x64_f16 v[212:215], v[220:223], v[98:105], v191
	s_nop 4
	v_add_f32_e32 v224, v200, v201
	v_add_f32_e32 v225, v204, v205
	v_add_f32_e32 v226, v208, v209
	v_add_f32_e32 v227, v212, v213
	v_cndmask_b32_e64 v172, v225, v224, s[6:7]
	v_cndmask_b32_e64 v172, v172, v226, s[0:1]
	v_cndmask_b32_e64 v172, v172, v227, s[4:5]
	v_exp_f32_e32 v172, v172
	s_nop 0
	v_add_f32_e32 v172, 1.0, v172
	v_rcp_f32_e32 v172, v172
	s_nop 0
	v_fmac_f32_e32 v137, v172, v136
	s_nop 1
	v_add_f32_dpp v136, v137, v137 quad_perm:[1,0,3,2] row_mask:0xf bank_mask:0xf bound_ctrl:1
	s_nop 1
	v_add_f32_dpp v136, v136, v136 quad_perm:[2,3,0,1] row_mask:0xf bank_mask:0xf bound_ctrl:1
	s_nop 1
	v_add_f32_dpp v136, v136, v136 row_half_mirror row_mask:0xf bank_mask:0xf bound_ctrl:1
	v_cvt_f16_f32_e32 v137, v136
	ds_write_b16 v150, v137
	s_waitcnt lgkmcnt(0)
	s_barrier
	ds_read_b128 v[156:159], v147
	ds_read_b32 v137, v134 offset:160
	v_add_f32_e32 v135, v135, v136
	s_waitcnt lgkmcnt(1)
	v_mfma_f32_16x16x32_f16 v[130:133], v[156:159], v[2:5], v[130:133]
	v_mfma_f32_16x16x32_f16 v[152:155], v[156:159], v[22:25], v[152:155]
	s_nop 7
	v_cndmask_b32_e64 v156, v130, v152, s[0:1]
	v_exp_f32_e64 v158, -|v156|
	v_max_f32 v159, 0, v156
	v_add_f32 v158, 1.0, v158
	v_log_f32 v158, v158
	s_nop 0
	v_fma_mixlo_f16 v157, v158, 1.0, v159
	ds_write_b16 v148, v157
	v_mov_b32_e32 v192, v106
	v_mov_b32_e32 v193, 0
	v_mov_b32_e32 v196, v110
	v_mov_b32_e32 v197, 0
	v_mul_f32 v136, -2.0, v137
	s_waitcnt lgkmcnt(0)
	s_barrier
	ds_read_b128 v[216:219], v139
	s_nop 2
	ds_read_b128 v[220:223], v141
	s_waitcnt lgkmcnt(1)
	v_smfmac_f32_16x16x64_f16 v[192:195], v[216:219], v[6:13], v191
	v_smfmac_f32_16x16x64_f16 v[196:199], v[216:219], v[26:33], v191
	s_waitcnt lgkmcnt(0)
	v_smfmac_f32_16x16x64_f16 v[192:195], v[220:223], v[14:21], v191
	v_smfmac_f32_16x16x64_f16 v[196:199], v[220:223], v[34:41], v191
	s_nop 6
	v_add_f32_e32 v224, v192, v193
	v_add_f32_e32 v225, v196, v197
	v_cndmask_b32_e64 v156, v224, v225, s[0:1]
	v_exp_f32_e64 v158, -|v156|
	v_max_f32 v159, 0, v156
	v_add_f32 v158, 1.0, v158
	v_log_f32 v158, v158
	s_nop 0
	v_fma_mixlo_f16 v157, v158, 1.0, v159
	ds_write_b16 v149, v157
	v_mov_b32_e32 v200, v114
	v_mov_b32_e32 v201, 0
	v_mov_b32_e32 v204, v118
	v_mov_b32_e32 v205, 0
	v_mov_b32_e32 v208, v122
	v_mov_b32_e32 v209, 0
	v_mov_b32_e32 v212, v126
	v_mov_b32_e32 v213, 0
	s_waitcnt lgkmcnt(0)
	s_barrier
	ds_read_b128 v[216:219], v143
	s_nop 2
	ds_read_b128 v[220:223], v145
	s_waitcnt lgkmcnt(1)
	v_smfmac_f32_16x16x64_f16 v[200:203], v[216:219], v[42:49], v191
	v_smfmac_f32_16x16x64_f16 v[204:207], v[216:219], v[58:65], v191
	v_smfmac_f32_16x16x64_f16 v[208:211], v[216:219], v[74:81], v191
	v_smfmac_f32_16x16x64_f16 v[212:215], v[216:219], v[90:97], v191
	s_waitcnt lgkmcnt(0)
	v_smfmac_f32_16x16x64_f16 v[200:203], v[220:223], v[50:57], v191
	v_smfmac_f32_16x16x64_f16 v[204:207], v[220:223], v[66:73], v191
	v_smfmac_f32_16x16x64_f16 v[208:211], v[220:223], v[82:89], v191
	v_smfmac_f32_16x16x64_f16 v[212:215], v[220:223], v[98:105], v191
	s_nop 4
	v_add_f32_e32 v224, v200, v201
	v_add_f32_e32 v225, v204, v205
	v_add_f32_e32 v226, v208, v209
	v_add_f32_e32 v227, v212, v213
	v_cndmask_b32_e64 v172, v225, v224, s[6:7]
	v_cndmask_b32_e64 v172, v172, v226, s[0:1]
	v_cndmask_b32_e64 v172, v172, v227, s[4:5]
	v_exp_f32_e32 v172, v172
	s_nop 0
	v_add_f32_e32 v172, 1.0, v172
	v_rcp_f32_e32 v172, v172
	s_nop 0
	v_fmac_f32_e32 v137, v172, v136
	s_nop 1
	v_add_f32_dpp v136, v137, v137 quad_perm:[1,0,3,2] row_mask:0xf bank_mask:0xf bound_ctrl:1
	s_nop 1
	v_add_f32_dpp v136, v136, v136 quad_perm:[2,3,0,1] row_mask:0xf bank_mask:0xf bound_ctrl:1
	s_nop 1
	v_add_f32_dpp v136, v136, v136 row_half_mirror row_mask:0xf bank_mask:0xf bound_ctrl:1
	v_cvt_f16_f32_e32 v137, v136
	ds_write_b16 v150, v137
	s_waitcnt lgkmcnt(0)
	s_barrier
	ds_read_b128 v[156:159], v147
	ds_read_b32 v137, v134 offset:192
	v_add_f32_e32 v135, v135, v136
	s_waitcnt lgkmcnt(1)
	v_mfma_f32_16x16x32_f16 v[130:133], v[156:159], v[2:5], v[130:133]
	v_mfma_f32_16x16x32_f16 v[154:157], v[156:159], v[22:25], v[152:155]
	s_nop 7
	v_cndmask_b32_e64 v152, v130, v154, s[0:1]
	v_exp_f32_e64 v158, -|v152|
	v_max_f32 v159, 0, v152
	v_add_f32 v158, 1.0, v158
	v_log_f32 v158, v158
	s_nop 0
	v_fma_mixlo_f16 v153, v158, 1.0, v159
	ds_write_b16 v148, v153
	v_mov_b32_e32 v192, v106
	v_mov_b32_e32 v193, 0
	v_mov_b32_e32 v196, v110
	v_mov_b32_e32 v197, 0
	v_mul_f32 v136, -2.0, v137
	s_waitcnt lgkmcnt(0)
	s_barrier
	ds_read_b128 v[216:219], v139
	s_nop 2
	ds_read_b128 v[220:223], v141
	s_waitcnt lgkmcnt(1)
	v_smfmac_f32_16x16x64_f16 v[192:195], v[216:219], v[6:13], v191
	v_smfmac_f32_16x16x64_f16 v[196:199], v[216:219], v[26:33], v191
	s_waitcnt lgkmcnt(0)
	v_smfmac_f32_16x16x64_f16 v[192:195], v[220:223], v[14:21], v191
	v_smfmac_f32_16x16x64_f16 v[196:199], v[220:223], v[34:41], v191
	s_nop 6
	v_add_f32_e32 v224, v192, v193
	v_add_f32_e32 v225, v196, v197
	v_cndmask_b32_e64 v152, v224, v225, s[0:1]
	v_exp_f32_e64 v158, -|v152|
	v_max_f32 v159, 0, v152
	v_add_f32 v158, 1.0, v158
	v_log_f32 v158, v158
	s_nop 0
	v_fma_mixlo_f16 v153, v158, 1.0, v159
	ds_write_b16 v149, v153
	v_mov_b32_e32 v200, v114
	v_mov_b32_e32 v201, 0
	v_mov_b32_e32 v204, v118
	v_mov_b32_e32 v205, 0
	v_mov_b32_e32 v208, v122
	v_mov_b32_e32 v209, 0
	v_mov_b32_e32 v212, v126
	v_mov_b32_e32 v213, 0
	s_waitcnt lgkmcnt(0)
	s_barrier
	ds_read_b128 v[216:219], v143
	s_nop 2
	ds_read_b128 v[220:223], v145
	s_waitcnt lgkmcnt(1)
	v_smfmac_f32_16x16x64_f16 v[200:203], v[216:219], v[42:49], v191
	v_smfmac_f32_16x16x64_f16 v[204:207], v[216:219], v[58:65], v191
	v_smfmac_f32_16x16x64_f16 v[208:211], v[216:219], v[74:81], v191
	v_smfmac_f32_16x16x64_f16 v[212:215], v[216:219], v[90:97], v191
	s_waitcnt lgkmcnt(0)
	v_smfmac_f32_16x16x64_f16 v[200:203], v[220:223], v[50:57], v191
	v_smfmac_f32_16x16x64_f16 v[204:207], v[220:223], v[66:73], v191
	v_smfmac_f32_16x16x64_f16 v[208:211], v[220:223], v[82:89], v191
	v_smfmac_f32_16x16x64_f16 v[212:215], v[220:223], v[98:105], v191
	s_nop 4
	v_add_f32_e32 v224, v200, v201
	v_add_f32_e32 v225, v204, v205
	v_add_f32_e32 v226, v208, v209
	v_add_f32_e32 v227, v212, v213
	v_cndmask_b32_e64 v152, v225, v224, s[6:7]
	v_cndmask_b32_e64 v152, v152, v226, s[0:1]
	v_cndmask_b32_e64 v152, v152, v227, s[4:5]
	v_exp_f32_e32 v152, v152
	s_nop 0
	v_add_f32_e32 v152, 1.0, v152
	v_rcp_f32_e32 v152, v152
	s_nop 0
	v_fmac_f32_e32 v137, v152, v136
	s_nop 1
	v_add_f32_dpp v136, v137, v137 quad_perm:[1,0,3,2] row_mask:0xf bank_mask:0xf bound_ctrl:1
	s_nop 1
	v_add_f32_dpp v136, v136, v136 quad_perm:[2,3,0,1] row_mask:0xf bank_mask:0xf bound_ctrl:1
	s_nop 1
	v_add_f32_dpp v136, v136, v136 row_half_mirror row_mask:0xf bank_mask:0xf bound_ctrl:1
	v_cvt_f16_f32_e32 v137, v136
	ds_write_b16 v150, v137
	s_waitcnt lgkmcnt(0)
	s_barrier
	ds_read_b128 v[158:161], v147
	v_add_f32_e32 v152, v135, v136
	ds_read_b32 v153, v134 offset:224
	s_addk_i32 s3, 0x100
	s_cmpk_eq_u32 s3, 0xfa20
	s_waitcnt lgkmcnt(1)
	v_mfma_f32_16x16x32_f16 v[130:133], v[158:161], v[2:5], v[130:133]
	v_mfma_f32_16x16x32_f16 v[134:137], v[158:161], v[22:25], v[154:157]
	s_nop 7
	v_cndmask_b32_e64 v154, v130, v134, s[0:1]
	s_cbranch_scc0 .LBB0_21
	s_and_saveexec_b64 s[0:1], vcc
	ds_write_b32 v1, v152
	s_or_b64 exec, exec, s[0:1]
	v_cmp_gt_u32_e32 vcc, 10, v0
	s_waitcnt lgkmcnt(0)
	s_barrier
	s_and_saveexec_b64 s[0:1], vcc
	s_cbranch_execz .LBB0_28
	v_lshlrev_b32_e32 v1, 2, v0
	global_load_dword v1, v1, s[12:13]
	v_mov_b32_e32 v139, 0
	v_lshl_add_u64 v[2:3], s[10:11], 0, v[138:139]
	v_lshl_add_u64 v[2:3], v[2:3], 0, 28
	s_mov_b32 s0, 0

	.amdhsa_kernel _Z11ncde_kernelPKfS0_S0_S0_S0_S0_S0_S0_S0_S0_S0_S0_S0_S0_S0_S0_S0_S0_S0_Pf
		.amdhsa_group_segment_fixed_size 79040
		.amdhsa_private_segment_fixed_size 0
		.amdhsa_kernarg_size 160
		.amdhsa_user_sgpr_count 2
		.amdhsa_user_sgpr_dispatch_ptr 0
		.amdhsa_user_sgpr_queue_ptr 0
		.amdhsa_user_sgpr_kernarg_segment_ptr 1
		.amdhsa_user_sgpr_dispatch_id 0
		.amdhsa_user_sgpr_kernarg_preload_length 0
		.amdhsa_user_sgpr_kernarg_preload_offset 0
		.amdhsa_user_sgpr_private_segment_size 0
		.amdhsa_uses_dynamic_stack 0
		.amdhsa_enable_private_segment 0
		.amdhsa_system_sgpr_workgroup_id_x 1
		.amdhsa_system_sgpr_workgroup_id_y 0
		.amdhsa_system_sgpr_workgroup_id_z 0
		.amdhsa_system_sgpr_workgroup_info 0
		.amdhsa_system_vgpr_workitem_id 0
		.amdhsa_next_free_vgpr 248
		.amdhsa_next_free_sgpr 96
		.amdhsa_accum_offset 248
		.amdhsa_reserve_vcc 1
		.amdhsa_float_round_mode_32 0
		.amdhsa_float_round_mode_16_64 0
		.amdhsa_float_denorm_mode_32 3
		.amdhsa_float_denorm_mode_16_64 3
		.amdhsa_dx10_clamp 1
		.amdhsa_ieee_mode 1
		.amdhsa_fp16_overflow 0
		.amdhsa_tg_split 0
		.amdhsa_exception_fp_ieee_invalid_op 0
		.amdhsa_exception_fp_denorm_src 0
		.amdhsa_exception_fp_ieee_div_zero 0
		.amdhsa_exception_fp_ieee_overflow 0
		.amdhsa_exception_fp_ieee_underflow 0
		.amdhsa_exception_fp_ieee_inexact 0
		.amdhsa_exception_int_div_zero 0
	.end_amdhsa_kernel

amdhsa.kernels:
  - .agpr_count:     0
    .args:
      - .actual_access:  read_only
        .address_space:  global
        .offset:         0
        .size:           8
        .value_kind:     global_buffer
      - .actual_access:  read_only
        .address_space:  global
        .offset:         8
        .size:           8
        .value_kind:     global_buffer
      - .actual_access:  read_only
        .address_space:  global
        .offset:         16
        .size:           8
        .value_kind:     global_buffer
      - .actual_access:  read_only
        .address_space:  global
        .offset:         24
        .size:           8
        .value_kind:     global_buffer
      - .actual_access:  read_only
        .address_space:  global
        .offset:         32
        .size:           8
        .value_kind:     global_buffer
      - .actual_access:  read_only
        .address_space:  global
        .offset:         40
        .size:           8
        .value_kind:     global_buffer
      - .actual_access:  read_only
        .address_space:  global
        .offset:         48
        .size:           8
        .value_kind:     global_buffer
      - .actual_access:  read_only
        .address_space:  global
        .offset:         56
        .size:           8
        .value_kind:     global_buffer
      - .actual_access:  read_only
        .address_space:  global
        .offset:         64
        .size:           8
        .value_kind:     global_buffer
      - .actual_access:  read_only
        .address_space:  global
        .offset:         72
        .size:           8
        .value_kind:     global_buffer
      - .actual_access:  read_only
        .address_space:  global
        .offset:         80
        .size:           8
        .value_kind:     global_buffer
      - .actual_access:  read_only
        .address_space:  global
        .offset:         88
        .size:           8
        .value_kind:     global_buffer
      - .actual_access:  read_only
        .address_space:  global
        .offset:         96
        .size:           8
        .value_kind:     global_buffer
      - .actual_access:  read_only
        .address_space:  global
        .offset:         104
        .size:           8
        .value_kind:     global_buffer
      - .actual_access:  read_only
        .address_space:  global
        .offset:         112
        .size:           8
        .value_kind:     global_buffer
      - .actual_access:  read_only
        .address_space:  global
        .offset:         120
        .size:           8
        .value_kind:     global_buffer
      - .actual_access:  read_only
        .address_space:  global
        .offset:         128
        .size:           8
        .value_kind:     global_buffer
      - .actual_access:  read_only
        .address_space:  global
        .offset:         136
        .size:           8
        .value_kind:     global_buffer
      - .actual_access:  read_only
        .address_space:  global
        .offset:         144
        .size:           8
        .value_kind:     global_buffer
      - .actual_access:  write_only
        .address_space:  global
        .offset:         152
        .size:           8
        .value_kind:     global_buffer
    .group_segment_fixed_size: 79040
    .kernarg_segment_align: 8
    .kernarg_segment_size: 160
    .language:       OpenCL C
    .language_version:
      - 2
      - 0
    .max_flat_workgroup_size: 256
    .name:           _Z11ncde_kernelPKfS0_S0_S0_S0_S0_S0_S0_S0_S0_S0_S0_S0_S0_S0_S0_S0_S0_S0_Pf
    .private_segment_fixed_size: 0
    .sgpr_count:     50
    .sgpr_spill_count: 0
    .symbol:         _Z11ncde_kernelPKfS0_S0_S0_S0_S0_S0_S0_S0_S0_S0_S0_S0_S0_S0_S0_S0_S0_S0_Pf.kd
    .uniform_work_group_size: 1
    .uses_dynamic_stack: false
    .vgpr_count:     248
    .vgpr_spill_count: 0
    .wavefront_size: 64
